# gemm8 tile->XCD mapping: every XCD gets 4 rotary (q/k) + 4 plain (v/g) feature tiles x 4 token tiles (same L2 footprint), so no XCD holds only late-finishing tiles
# speedup vs baseline: 1.0367x; 1.0101x over previous
_Z5gemm8ILi0EEvPKtS1_ii7EpiArgs:
	s_load_dwordx4 s[8:11], s[0:1], 0x0
	s_waitcnt lgkmcnt(0)
	s_and_b32 s3, s2, 7
	s_lshr_b32 s6, s2, 3
	s_lshr_b32 s7, s3, 1
	s_lshl_b32 s7, s7, 2
	s_lshr_b32 s12, s6, 3
	s_add_i32 s7, s7, s12
	s_and_b32 s3, s3, 1
	s_lshl_b32 s3, s3, 2
	s_and_b32 s12, s6, 3
	s_add_i32 s3, s3, s12
	s_bfe_u32 s12, s6, 0x10002
	s_lshl_b32 s12, s12, 3
	s_add_i32 s24, s3, s12
	v_and_b32_e32 v2, 32, v0
	v_bfe_u32 v14, v0, 2, 4
	v_and_b32_e32 v16, 64, v0
	v_mov_b32_e32 v131, 0
	v_mov_b32_e32 v19, v131
	v_mov_b32_e32 v21, v131
	v_lshrrev_b32_e32 v145, 8, v0
	s_ashr_i32 s25, s24, 2
	s_cmp_eq_u32 s25, 2
	s_cselect_b64 s[4:5], -1, 0
	s_and_b64 s[2:3], s[4:5], exec
	s_cselect_b32 s2, s24, s7
	s_cselect_b32 s20, s9, s11
	s_cselect_b32 s21, s8, s10
	s_cselect_b32 s14, s7, s24
	s_lshl_b32 s6, s2, 8
	s_ashr_i32 s7, s6, 31
	s_lshl_b64 s[2:3], s[6:7], 11
	s_add_u32 s12, s21, s2
	v_lshlrev_b32_e32 v1, 4, v0
	s_addc_u32 s13, s20, s3
	s_add_i32 s22, 0, 0x10000
	v_add_u32_e32 v152, s22, v1
	v_or_b32_e32 v17, 0x2000, v1
	v_readfirstlane_b32 s7, v152
	v_bitop3_b32 v15, v1, v2, 48 bitop3:0x6c
	v_lshrrev_b32_e32 v2, 3, v0
	s_mov_b32 m0, s7
	v_lshrrev_b32_e32 v6, 7, v17
	s_movk_i32 s7, 0x70
	v_or_b32_e32 v130, v15, v16
	v_and_or_b32 v2, v2, 48, v14
	v_and_or_b32 v6, v6, s7, v14
	v_lshl_add_u64 v[4:5], s[12:13], 0, v[130:131]
	v_lshlrev_b32_e32 v18, 11, v2
	v_lshlrev_b32_e32 v20, 11, v6
	v_add_u32_e32 v6, s22, v17
	v_lshl_add_u64 v[2:3], v[4:5], 0, v[18:19]
	v_readfirstlane_b32 s7, v6
	s_and_b64 s[12:13], s[4:5], exec
	global_load_lds_dwordx4 v[2:3], off
	s_mov_b32 m0, s7
	s_cselect_b32 s7, s11, s9
	s_cselect_b32 s23, s10, s8
	s_lshl_b32 s12, s14, 8
	s_ashr_i32 s13, s12, 31
	s_lshl_b64 s[18:19], s[12:13], 11
	s_add_u32 s8, s23, s18
	s_addc_u32 s9, s7, s19
	v_add_u32_e32 v153, 0, v1
	v_lshl_add_u64 v[4:5], v[4:5], 0, v[20:21]
	v_lshl_add_u64 v[8:9], s[8:9], 0, v[130:131]
	v_readfirstlane_b32 s8, v153
	v_add_u32_e32 v155, 0x2000, v153
	global_load_lds_dwordx4 v[4:5], off
	v_lshl_add_u64 v[6:7], v[8:9], 0, v[18:19]
	s_mov_b32 m0, s8
	v_readfirstlane_b32 s8, v155
	global_load_lds_dwordx4 v[6:7], off
	s_mov_b32 m0, s8
	s_or_b32 s8, s6, 0x80
	s_ashr_i32 s9, s8, 31
	s_lshl_b64 s[8:9], s[8:9], 11
	s_add_u32 s8, s21, s8
	s_addc_u32 s9, s20, s9
	s_add_i32 s13, 0, 0x14000
	v_add_u32_e32 v156, s13, v1
	v_lshl_add_u64 v[8:9], v[8:9], 0, v[20:21]
	v_lshl_add_u64 v[12:13], s[8:9], 0, v[130:131]
	v_readfirstlane_b32 s8, v156
	v_add_u32_e32 v22, s13, v17
	global_load_lds_dwordx4 v[8:9], off
	v_lshl_add_u64 v[10:11], v[12:13], 0, v[18:19]
	s_mov_b32 m0, s8
	v_readfirstlane_b32 s8, v22
	global_load_lds_dwordx4 v[10:11], off
	s_mov_b32 m0, s8
	s_or_b32 s8, s12, 0x80
	s_ashr_i32 s9, s8, 31
	s_lshl_b64 s[8:9], s[8:9], 11
	s_add_u32 s8, s23, s8
	s_addc_u32 s9, s7, s9
	v_add_u32_e32 v158, 0x4000, v153
	v_lshl_add_u64 v[12:13], v[12:13], 0, v[20:21]
	v_lshl_add_u64 v[22:23], s[8:9], 0, v[130:131]
	v_readfirstlane_b32 s8, v158
	v_add_u32_e32 v159, 0x6000, v153
	global_load_lds_dwordx4 v[12:13], off
	v_lshl_add_u64 v[132:133], v[22:23], 0, v[18:19]
	s_mov_b32 m0, s8
	v_readfirstlane_b32 s8, v159
	global_load_lds_dwordx4 v[132:133], off
	v_lshl_add_u64 v[134:135], v[22:23], 0, v[20:21]
	s_mov_b32 m0, s8
	v_cmp_eq_u32_e32 vcc, 1, v145
	global_load_lds_dwordx4 v[134:135], off
	s_load_dwordx2 s[16:17], s[0:1], 0x30
	s_load_dwordx2 s[14:15], s[0:1], 0x40
	s_and_saveexec_b64 s[8:9], vcc
	s_cbranch_execz .LBB15_6
	s_barrier
